# phase-1 prologue: adaLN partial-sum loads all in flight, scale-chain adds after one counted wait; on top of v26
# speedup vs baseline: 1.0092x; 1.0019x over previous
; __device__ __forceinline__ void phase1(KP kp, LAS unsigned char* lds, int wave, int bid, int G) {
;     ...
;     for (int c = tid; c < 2048; c += 512) { float sh = b_ada[c], sc = b_ada[2048 + c];
;         for (int r = 0; r < 16; ++r) { sh += modp[r * 12288 + c]; sc += modp[r * 12288 + 2048 + c]; }
;         A1[c] = n1g[c] * (1.0f + sc); B1[c] = sh; }
.LBB0_125:
	v_ashrrev_i32_e32 v7, 31, v2
	v_mov_b32_e32 v6, v2
	v_lshlrev_b64 v[12:13], 2, v[6:7]
	v_ashrrev_i32_e32 v5, 31, v3
	v_mov_b32_e32 v4, v3
	v_lshl_add_u64 v[10:11], s[8:9], 0, v[12:13]
	v_lshlrev_b64 v[14:15], 2, v[4:5]
	s_waitcnt vmcnt(8)
	v_add_co_u32_e32 v24, vcc, s5, v10
	v_lshl_add_u64 v[8:9], s[8:9], 0, v[14:15]
	v_lshl_add_u64 v[6:7], s[26:27], 0, v[12:13]
	v_lshl_add_u64 v[18:19], s[10:11], 0, v[12:13]
	v_addc_co_u32_e32 v25, vcc, 0, v11, vcc
	v_lshl_add_u64 v[4:5], s[26:27], 0, v[14:15]
	v_lshl_add_u64 v[16:17], s[10:11], 0, v[14:15]
	global_load_dword v12, v[10:11], off
	global_load_dword v13, v[8:9], off
	global_load_dword v14, v[6:7], off
	global_load_dword v15, v[4:5], off
	s_nop 0
	global_load_dword v10, v[18:19], off
	v_add_co_u32_e32 v18, vcc, s5, v8
	v_add_u32_e32 v23, -2, v23
	s_nop 0
	v_addc_co_u32_e32 v19, vcc, 0, v9, vcc
	v_add_co_u32_e32 v26, vcc, s5, v6
	global_load_dword v8, v[24:25], off
	global_load_dword v9, v[18:19], off
	v_addc_co_u32_e32 v27, vcc, 0, v7, vcc
	v_add_co_u32_e32 v24, vcc, s5, v4
	v_add_u32_e32 v3, 0x400, v3
	s_nop 0
	v_addc_co_u32_e32 v25, vcc, 0, v5, vcc
	v_add_co_u32_e32 v28, vcc, s17, v6
	global_load_dword v18, v[26:27], off
	global_load_dword v19, v[24:25], off
	v_addc_co_u32_e32 v29, vcc, 0, v7, vcc
	v_add_co_u32_e32 v24, vcc, s17, v4
	v_add_u32_e32 v2, 0x400, v2
	s_nop 0
	v_addc_co_u32_e32 v25, vcc, 0, v5, vcc
	v_add_co_u32_e32 v26, vcc, s18, v6
	global_load_dword v28, v[28:29], off
	s_nop 0
	global_load_dword v29, v[24:25], off
	v_addc_co_u32_e32 v27, vcc, 0, v7, vcc
	v_add_co_u32_e32 v24, vcc, s18, v4
	v_addc_co_u32_e32 v25, vcc, 0, v5, vcc
	v_add_co_u32_e32 v30, vcc, s19, v6
	global_load_dword v26, v[26:27], off
	s_nop 0
	global_load_dword v27, v[24:25], off
	v_addc_co_u32_e32 v31, vcc, 0, v7, vcc
	v_add_co_u32_e32 v24, vcc, s19, v4
	v_addc_co_u32_e32 v25, vcc, 0, v5, vcc
	v_add_co_u32_e32 v32, vcc, s20, v6
	global_load_dword v30, v[30:31], off
	s_nop 0
	global_load_dword v31, v[24:25], off
	v_addc_co_u32_e32 v33, vcc, 0, v7, vcc
	v_add_co_u32_e32 v24, vcc, s20, v4
	s_nop 1
	v_addc_co_u32_e32 v25, vcc, 0, v5, vcc
	v_add_co_u32_e32 v34, vcc, s21, v6
	global_load_dword v32, v[32:33], off
	s_nop 0
	global_load_dword v33, v[24:25], off
	v_addc_co_u32_e32 v35, vcc, 0, v7, vcc
	v_add_co_u32_e32 v24, vcc, s21, v4
	v_addc_co_u32_e32 v25, vcc, 0, v5, vcc
	v_add_co_u32_e32 v36, vcc, s22, v6
	global_load_dword v34, v[34:35], off
	s_nop 0
	global_load_dword v35, v[24:25], off
	v_addc_co_u32_e32 v37, vcc, 0, v7, vcc
	v_add_co_u32_e32 v24, vcc, s22, v4
	s_nop 1
	v_addc_co_u32_e32 v25, vcc, 0, v5, vcc
	v_add_co_u32_e32 v38, vcc, s23, v6
	global_load_dword v36, v[36:37], off
	s_nop 0
	global_load_dword v37, v[24:25], off
	v_addc_co_u32_e32 v39, vcc, 0, v7, vcc
	v_add_co_u32_e32 v24, vcc, s23, v4
	v_addc_co_u32_e32 v25, vcc, 0, v5, vcc
	v_add_co_u32_e32 v40, vcc, s24, v6
	global_load_dword v38, v[38:39], off
	s_nop 0
	global_load_dword v39, v[24:25], off
	v_addc_co_u32_e32 v41, vcc, 0, v7, vcc
	v_add_co_u32_e32 v24, vcc, s24, v4
	s_nop 1
	v_addc_co_u32_e32 v25, vcc, 0, v5, vcc
	v_add_co_u32_e32 v42, vcc, s25, v6
	global_load_dword v40, v[40:41], off
	s_nop 0
	global_load_dword v41, v[24:25], off
	v_addc_co_u32_e32 v43, vcc, 0, v7, vcc
	v_add_co_u32_e32 v24, vcc, s25, v4
	v_addc_co_u32_e32 v25, vcc, 0, v5, vcc
	v_add_co_u32_e32 v44, vcc, s30, v6
	global_load_dword v42, v[42:43], off
	s_nop 0
	global_load_dword v43, v[24:25], off
	v_addc_co_u32_e32 v45, vcc, 0, v7, vcc
	v_add_co_u32_e32 v24, vcc, s30, v4
	s_nop 1
	v_addc_co_u32_e32 v25, vcc, 0, v5, vcc
	v_add_co_u32_e32 v46, vcc, s31, v6
	global_load_dword v44, v[44:45], off
	s_nop 0
	global_load_dword v45, v[24:25], off
	v_addc_co_u32_e32 v47, vcc, 0, v7, vcc
	v_add_co_u32_e32 v24, vcc, s31, v4
	v_addc_co_u32_e32 v25, vcc, 0, v5, vcc
	v_add_co_u32_e32 v48, vcc, s34, v6
	global_load_dword v46, v[46:47], off
	s_nop 0
	global_load_dword v47, v[24:25], off
	v_addc_co_u32_e32 v49, vcc, 0, v7, vcc
	v_add_co_u32_e32 v24, vcc, s34, v4
	s_nop 1
	v_addc_co_u32_e32 v25, vcc, 0, v5, vcc
	v_add_co_u32_e32 v50, vcc, s35, v6
	global_load_dword v48, v[48:49], off
	s_nop 0
	global_load_dword v49, v[24:25], off
	v_addc_co_u32_e32 v51, vcc, 0, v7, vcc
	v_add_co_u32_e32 v24, vcc, s35, v4
	v_addc_co_u32_e32 v25, vcc, 0, v5, vcc
	v_add_co_u32_e32 v52, vcc, s36, v6
	global_load_dword v50, v[50:51], off
	s_nop 0
	global_load_dword v51, v[24:25], off
	v_addc_co_u32_e32 v53, vcc, 0, v7, vcc
	v_add_co_u32_e32 v24, vcc, s36, v4
	s_nop 1
	v_addc_co_u32_e32 v25, vcc, 0, v5, vcc
	v_add_co_u32_e32 v54, vcc, s37, v6
	global_load_dword v52, v[52:53], off
	s_nop 0
	global_load_dword v53, v[24:25], off
	v_addc_co_u32_e32 v55, vcc, 0, v7, vcc
	v_add_co_u32_e32 v24, vcc, s37, v4
	s_waitcnt vmcnt(30)
; __device__ __forceinline__ void phase1(KP kp, LAS unsigned char* lds, int wave, int bid, int G) {
;     ...
;     for (int c = tid; c < 2048; c += 512) { float sh = b_ada[c], sc = b_ada[2048 + c];
;         for (int r = 0; r < 16; ++r) { sh += modp[r * 12288 + c]; sc += modp[r * 12288 + 2048 + c]; }
;         A1[c] = n1g[c] * (1.0f + sc); B1[c] = sh; }
	v_addc_co_u32_e32 v25, vcc, 0, v5, vcc
	v_add_co_u32_e32 v56, vcc, s38, v6
	global_load_dword v54, v[54:55], off
	s_nop 0
	global_load_dword v55, v[24:25], off
	v_addc_co_u32_e32 v57, vcc, 0, v7, vcc
	v_add_co_u32_e32 v24, vcc, s38, v4
	s_nop 1
	v_addc_co_u32_e32 v25, vcc, 0, v5, vcc
	v_add_co_u32_e32 v58, vcc, s39, v6
	global_load_dword v56, v[56:57], off
	s_nop 0
	global_load_dword v57, v[24:25], off
	v_addc_co_u32_e32 v59, vcc, 0, v7, vcc
	v_add_co_u32_e32 v24, vcc, s39, v4
	v_addc_co_u32_e32 v25, vcc, 0, v5, vcc
	v_add_co_u32_e32 v60, vcc, s40, v6
	global_load_dword v58, v[58:59], off
	s_nop 0
	global_load_dword v59, v[24:25], off
	v_addc_co_u32_e32 v61, vcc, 0, v7, vcc
	v_add_co_u32_e32 v24, vcc, s40, v4
	s_nop 1
	v_addc_co_u32_e32 v25, vcc, 0, v5, vcc
	v_add_co_u32_e32 v62, vcc, s41, v6
	global_load_dword v60, v[60:61], off
	s_nop 0
	global_load_dword v61, v[24:25], off
	v_addc_co_u32_e32 v63, vcc, 0, v7, vcc
	v_add_co_u32_e32 v24, vcc, s41, v4
	v_addc_co_u32_e32 v25, vcc, 0, v5, vcc
	v_add_co_u32_e32 v66, vcc, s42, v6
	global_load_dword v62, v[62:63], off
	s_nop 0
	global_load_dword v63, v[24:25], off
	v_addc_co_u32_e32 v67, vcc, 0, v7, vcc
	v_add_co_u32_e32 v24, vcc, s42, v4
	s_nop 1
	v_addc_co_u32_e32 v25, vcc, 0, v5, vcc
	v_add_co_u32_e32 v68, vcc, s43, v6
	global_load_dword v66, v[66:67], off
	s_nop 0
	global_load_dword v67, v[24:25], off
	v_addc_co_u32_e32 v69, vcc, 0, v7, vcc
	v_add_co_u32_e32 v24, vcc, s43, v4
	v_addc_co_u32_e32 v25, vcc, 0, v5, vcc
	v_add_co_u32_e32 v70, vcc, s44, v6
	global_load_dword v68, v[68:69], off
	s_nop 0
	global_load_dword v69, v[24:25], off
	v_addc_co_u32_e32 v71, vcc, 0, v7, vcc
	v_add_co_u32_e32 v24, vcc, s44, v4
	s_nop 1
	v_addc_co_u32_e32 v25, vcc, 0, v5, vcc
	v_add_co_u32_e32 v72, vcc, s45, v6
	global_load_dword v70, v[70:71], off
	s_nop 0
	global_load_dword v71, v[24:25], off
	v_addc_co_u32_e32 v73, vcc, 0, v7, vcc
	v_add_co_u32_e32 v24, vcc, s45, v4
	v_addc_co_u32_e32 v25, vcc, 0, v5, vcc
	v_add_co_u32_e32 v74, vcc, s46, v6
	global_load_dword v72, v[72:73], off
	s_nop 0
	global_load_dword v73, v[24:25], off
	v_addc_co_u32_e32 v75, vcc, 0, v7, vcc
	v_add_co_u32_e32 v24, vcc, s46, v4
	s_nop 1
	v_addc_co_u32_e32 v25, vcc, 0, v5, vcc
	v_add_co_u32_e32 v76, vcc, s47, v6
	global_load_dword v74, v[74:75], off
	s_nop 0
	global_load_dword v75, v[24:25], off
	v_addc_co_u32_e32 v77, vcc, 0, v7, vcc
	v_add_co_u32_e32 v24, vcc, s47, v4
	v_addc_co_u32_e32 v25, vcc, 0, v5, vcc
	v_add_co_u32_e32 v78, vcc, s48, v6
	global_load_dword v76, v[76:77], off
	s_nop 0
	global_load_dword v77, v[24:25], off
	v_addc_co_u32_e32 v79, vcc, 0, v7, vcc
	v_add_co_u32_e32 v24, vcc, s48, v4
	s_nop 1
	v_addc_co_u32_e32 v25, vcc, 0, v5, vcc
	v_add_co_u32_e32 v80, vcc, s49, v6
	global_load_dword v78, v[78:79], off
	s_nop 0
	global_load_dword v79, v[24:25], off
	v_addc_co_u32_e32 v81, vcc, 0, v7, vcc
	v_add_co_u32_e32 v24, vcc, s49, v4
	v_addc_co_u32_e32 v25, vcc, 0, v5, vcc
	v_add_co_u32_e32 v82, vcc, s50, v6
	global_load_dword v80, v[80:81], off
	s_nop 0
	global_load_dword v81, v[24:25], off
	v_addc_co_u32_e32 v83, vcc, 0, v7, vcc
	v_add_co_u32_e32 v24, vcc, s50, v4
	s_nop 1
	v_addc_co_u32_e32 v25, vcc, 0, v5, vcc
	v_add_co_u32_e32 v84, vcc, s51, v6
	global_load_dword v82, v[82:83], off
	s_nop 0
	global_load_dword v83, v[24:25], off
	v_addc_co_u32_e32 v85, vcc, 0, v7, vcc
	v_add_co_u32_e32 v24, vcc, s51, v4
	v_addc_co_u32_e32 v25, vcc, 0, v5, vcc
	v_add_co_u32_e32 v6, vcc, s52, v6
	global_load_dword v84, v[84:85], off
	s_nop 0
	global_load_dword v85, v[24:25], off
	v_addc_co_u32_e32 v7, vcc, 0, v7, vcc
	v_add_co_u32_e32 v4, vcc, s52, v4
	s_nop 1
	v_addc_co_u32_e32 v5, vcc, 0, v5, vcc
	global_load_dword v6, v[6:7], off
	s_nop 0
	global_load_dword v7, v[4:5], off
	global_load_dword v11, v[16:17], off
	s_waitcnt vmcnt(5)
	v_pk_add_f32 v[8:9], v[8:9], v[18:19]
	s_nop 0
	v_pk_add_f32 v[8:9], v[8:9], v[26:27]
	s_nop 0
	v_pk_add_f32 v[8:9], v[8:9], v[32:33]
	s_nop 0
	v_pk_add_f32 v[8:9], v[8:9], v[36:37]
	s_nop 0
	v_pk_add_f32 v[8:9], v[8:9], v[40:41]
	s_nop 0
	v_pk_add_f32 v[8:9], v[8:9], v[44:45]
	s_nop 0
	v_pk_add_f32 v[8:9], v[8:9], v[48:49]
	s_nop 0
	v_pk_add_f32 v[8:9], v[8:9], v[52:53]
	s_nop 0
	v_pk_add_f32 v[8:9], v[8:9], v[56:57]
	s_nop 0
	v_pk_add_f32 v[8:9], v[8:9], v[60:61]
	s_nop 0
	v_pk_add_f32 v[8:9], v[8:9], v[66:67]
	s_nop 0
	v_pk_add_f32 v[8:9], v[8:9], v[70:71]
	s_nop 0
	v_pk_add_f32 v[8:9], v[8:9], v[74:75]
	s_nop 0
	v_pk_add_f32 v[8:9], v[8:9], v[78:79]
	s_nop 0
	v_pk_add_f32 v[8:9], v[8:9], v[82:83]
	s_nop 0
	v_pk_add_f32 v[4:5], v[12:13], v[14:15]
	v_cmp_eq_u32_e32 vcc, 0, v23
	v_pk_add_f32 v[4:5], v[4:5], v[28:29]
	s_or_b64 s[28:29], vcc, s[28:29]
	v_pk_add_f32 v[4:5], v[4:5], v[30:31]
	s_nop 0
	v_pk_add_f32 v[4:5], v[4:5], v[34:35]
	s_nop 0
	v_pk_add_f32 v[4:5], v[4:5], v[38:39]
	s_nop 0
	v_pk_add_f32 v[4:5], v[4:5], v[42:43]
	s_nop 0
	v_pk_add_f32 v[4:5], v[4:5], v[46:47]
	s_nop 0
	v_pk_add_f32 v[4:5], v[4:5], v[50:51]
	s_nop 0
	v_pk_add_f32 v[4:5], v[4:5], v[54:55]
	s_nop 0
	v_pk_add_f32 v[4:5], v[4:5], v[58:59]
	s_nop 0
	v_pk_add_f32 v[4:5], v[4:5], v[62:63]
	s_nop 0
	v_pk_add_f32 v[4:5], v[4:5], v[68:69]
	s_nop 0
	v_pk_add_f32 v[4:5], v[4:5], v[72:73]
	s_nop 0
	v_pk_add_f32 v[4:5], v[4:5], v[76:77]
	s_nop 0
	v_pk_add_f32 v[4:5], v[4:5], v[80:81]
	s_waitcnt vmcnt(3)
	v_pk_add_f32 v[4:5], v[4:5], v[84:85]
	ds_write2st64_b32 v22, v4, v5 offset0:32 offset1:40
	s_waitcnt vmcnt(1)
	v_pk_add_f32 v[4:5], v[8:9], v[6:7]
	s_nop 0
	v_pk_add_f32 v[4:5], v[4:5], 1.0 op_sel_hi:[1,0]
	s_waitcnt vmcnt(0)
	v_pk_mul_f32 v[4:5], v[10:11], v[4:5]
	ds_write2st64_b32 v22, v4, v5 offset1:8
	v_add_u32_e32 v22, 0x1000, v22
	s_andn2_b64 exec, exec, s[28:29]
	s_cbranch_execnz .LBB0_125
	s_or_b64 exec, exec, s[28:29]
	v_cmp_ne_u32_e32 vcc, v20, v21
	v_lshl_add_u32 v2, v21, 9, v0
	s_orn2_b64 s[26:27], vcc, exec
